# barrier entry: wave 2 (idle until the closing barrier) loads the following code (rest of the barrier + next phase, up to 40 KB, kept inside .text) so the next phase's first instruction fetches hit the
# speedup vs baseline: 1.0234x; 1.0038x over previous
.Lxinvw_0:
	s_cmp_lg_u32 s4, 0x80
	s_cbranch_scc1 .Lcwarm_0
	s_getpc_b64 s[4:5]
	v_mbcnt_lo_u32_b32 v0, -1, 0
	v_mbcnt_hi_u32_b32 v0, -1, v0
	v_lshlrev_b32_e32 v0, 7, v0
	global_load_dword v1, v0, s[4:5]
	v_add_u32_e32 v0, 0x2000, v0
	global_load_dword v1, v0, s[4:5]
	v_add_u32_e32 v0, 0x2000, v0
	global_load_dword v1, v0, s[4:5]
	v_add_u32_e32 v0, 0x2000, v0
	global_load_dword v1, v0, s[4:5]
	v_add_u32_e32 v0, 0x2000, v0
	global_load_dword v1, v0, s[4:5]
	s_waitcnt vmcnt(0)

.Lxinvw_1:
	s_cmp_lg_u32 s6, 0x80
	s_cbranch_scc1 .Lcwarm_1
	s_getpc_b64 s[6:7]
	v_mbcnt_lo_u32_b32 v0, -1, 0
	v_mbcnt_hi_u32_b32 v0, -1, v0
	v_lshlrev_b32_e32 v0, 7, v0
	global_load_dword v1, v0, s[6:7]
	v_add_u32_e32 v0, 0x2000, v0
	global_load_dword v1, v0, s[6:7]
	v_add_u32_e32 v0, 0x2000, v0
	global_load_dword v1, v0, s[6:7]
	v_add_u32_e32 v0, 0x2000, v0
	global_load_dword v1, v0, s[6:7]
	v_add_u32_e32 v0, 0x2000, v0
	global_load_dword v1, v0, s[6:7]
	s_waitcnt vmcnt(0)

.Lxinvw_9:
	s_cmp_lg_u32 s4, 0x80
	s_cbranch_scc1 .Lcwarm_9
	s_getpc_b64 s[4:5]
	v_mbcnt_lo_u32_b32 v0, -1, 0
	v_mbcnt_hi_u32_b32 v0, -1, v0
	v_lshlrev_b32_e32 v0, 7, v0
	global_load_dword v1, v0, s[4:5]
	v_add_u32_e32 v0, 0x2000, v0
	global_load_dword v1, v0, s[4:5]
	v_add_u32_e32 v0, 0x2000, v0
	global_load_dword v1, v0, s[4:5]
	s_waitcnt vmcnt(0)

.Lxinvw_10:
	s_cmp_lg_u32 s4, 0x80
	s_cbranch_scc1 .Lcwarm_10
	s_getpc_b64 s[4:5]
	v_mbcnt_lo_u32_b32 v0, -1, 0
	v_mbcnt_hi_u32_b32 v0, -1, v0
	v_lshlrev_b32_e32 v0, 7, v0
	global_load_dword v1, v0, s[4:5]
	v_add_u32_e32 v0, 0x2000, v0
	global_load_dword v1, v0, s[4:5]
	s_waitcnt vmcnt(0)

.Lxinvw_11:
	s_cmp_lg_u32 s6, 0x80
	s_cbranch_scc1 .Lcwarm_11
	s_getpc_b64 s[6:7]
	v_mbcnt_lo_u32_b32 v0, -1, 0
	v_mbcnt_hi_u32_b32 v0, -1, v0
	v_lshlrev_b32_e32 v0, 7, v0
	global_load_dword v1, v0, s[6:7]
	s_waitcnt vmcnt(0)
